# v21 plus converter DMA issue moved to the loader waves 4-7, read-back and stores stay on waves 0-3
# baseline (speedup 1.0000x reference)
; #define LAS __attribute__((address_space(3)))
; #define INF(i) ((const float*)arg_ptr(i))
; __device__ __forceinline__ int v_rd_base(int lane) { return ((lane & 3) << 3) | (((lane >> 2) & 3) << 6) | (((lane >> 4) & 1) << 5) | (((lane >> 5) & 1) << 8); }
; template <int layer>
; __device__ __forceinline__ void attn_phase(LAS unsigned char* lds) {
;     ...
;     const int tkp = (tid - 256) & 255; const unsigned kof0 = koff_n(tkp, 0), vof0 = voff_f(tkp, 0), rof0 = koff_r(tkp, 0);
;     const int kbn = r32 * 256 + ((hi * 16) ^ ((r32 & 7) << 4)), kbr0 = 16384 + r32 * 128 + ((hi * 16) ^ ((r32 & 7) << 4));
;     const unsigned ldsb = (unsigned)(uintptr_t)lds;
;     const int vb0 = (int)(unsigned)(uintptr_t)(lds + OFF_V) + v_rd_base(lane);
;     LAS float* wsl = (LAS float*)(lds + OFF_WS) + wid * 64; LAS float* li_l = wsl; LAS float* al_l = wsl + 32;
;     const float* cv_wgu = INF(layer == 0 ? 15 : 27); const float* cv_wdn = INF(layer == 0 ? 16 : 28); bf16* cv_gut = WSP(bf16, CV_MODE >= 2 ? WS_Q : WS_W_GUT); bf16* cv_dt = WSP(bf16, CV_MODE >= 2 ? WS_Q : WS_W_DT);
;     constexpr int CV_IG = 32 * 32, CV_ID = 8 * 64, CV_NIT = NEXP * (CV_IG + CV_ID);
;     int cv_it = (CV_MODE == 1) ? CV_NIT : bx * 4 + wid, cv_pend = -1; const int cv_stride = G * 4;
;     const unsigned cv_lds = (unsigned)(uintptr_t)(lds + OFF_CV) + (unsigned)(wid & 3) * 16384u;
.LBB0_525:
	s_or_b64 exec, exec, s[4:5]
	s_mov_b32 s0, 30
	s_waitcnt lgkmcnt(0)
	s_barrier
	s_ashr_i32 s1, s0, 31
	s_lshl_b64 s[0:1], s[0:1], 3
	s_add_u32 s0, s80, s0
	s_addc_u32 s1, s81, s1
	v_mov_b32_e32 v4, v0
	s_load_dwordx2 s[4:5], s[0:1], 0x0
	s_mov_b32 s9, s78
	v_readfirstlane_b32 s0, v4
	s_mov_b32 s28, s79
	s_mov_b32 s8, 8
	s_mov_b32 s6, 1
	s_ashr_i32 s14, s0, 6
	s_mov_b32 s0, 15
	s_ashr_i32 s1, s0, 31
	s_lshl_b64 s[0:1], s[0:1], 3
	s_add_u32 s0, s80, s0
	s_addc_u32 s1, s81, s1
	s_load_dwordx2 s[10:11], s[0:1], 0x0
	s_mov_b32 s0, 16
	s_ashr_i32 s1, s0, 31
	s_lshl_b64 s[0:1], s[0:1], 3
	s_add_u32 s0, s80, s0
	s_addc_u32 s1, s81, s1
	s_load_dwordx2 s[12:13], s[0:1], 0x0
	s_waitcnt lgkmcnt(0)
	s_add_u32 s0, s4, 0x3e00000
	s_addc_u32 s1, s5, 0
	s_add_u32 s2, s4, 0x13e00000
	s_addc_u32 s3, s5, 0
	s_lshl_b32 s7, s28, 2
	s_and_b32 s98, s14, 3
	s_add_i32 s15, s98, s7
	s_lshl_b32 s7, s14, 14
	s_and_b32 s7, s7, 0xc000
	v_writelane_b32 v252, s9, 9
	s_add_i32 s24, s7, 0
	s_lshl_b32 s22, s9, 2
	s_add_i32 s23, s24, 0x15000
	v_writelane_b32 v252, s79, 10
	s_mov_b32 s29, 0
	s_cmpk_gt_i32 s28, 0x1ff
	s_mov_b32 s33, -1
	v_writelane_b32 v252, s80, 11
	s_nop 1
	v_writelane_b32 v252, s81, 12
	s_cbranch_scc1 .LBB0_583
	s_add_u32 s7, s4, 0x64300000
	v_bfe_u32 v1, v4, 4, 4
	v_and_b32_e32 v3, 15, v4
	v_writelane_b32 v252, s7, 13
	s_addc_u32 s7, s5, 0
	v_bitop3_b32 v3, v1, v3, 15 bitop3:0x6c
	v_lshlrev_b32_e32 v1, 13, v1
	v_writelane_b32 v252, s7, 14
	s_add_u32 s7, s4, 0x31e00000
	v_lshl_or_b32 v1, v3, 4, v1
	v_lshrrev_b32_e32 v3, 5, v4
	v_lshrrev_b32_e32 v7, 1, v4
	v_writelane_b32 v252, s7, 15
	s_addc_u32 s7, s5, 0
	v_and_b32_e32 v3, 4, v3
	v_bfe_u32 v6, v4, 2, 2
	v_and_b32_e32 v7, 8, v7
	v_writelane_b32 v252, s7, 16
	s_add_u32 s7, s4, 0x42000000
	v_or3_b32 v3, v6, v7, v3
	v_and_b32_e32 v6, 0x60, v4
	v_lshlrev_b32_e32 v7, 3, v4
	v_writelane_b32 v252, s7, 17
	s_addc_u32 s7, s5, 0
	s_ashr_i32 s9, s8, 31
	v_and_or_b32 v6, v7, 24, v6
	s_lshl_b64 s[8:9], s[8:9], 3
	v_lshlrev_b32_e32 v6, 1, v6
	s_add_u32 s8, s80, s8
	v_lshl_or_b32 v181, v3, 13, v6
	v_bfe_u32 v3, v4, 3, 5
	v_writelane_b32 v252, s7, 18
	s_addc_u32 s9, s81, s9
	s_ashr_i32 s7, s6, 31
	v_lshrrev_b32_e32 v6, 1, v3
	v_xor_b32_e32 v6, v6, v4
	s_lshl_b64 s[6:7], s[6:7], 3
	v_bfe_u32 v5, v4, 5, 1
	v_lshlrev_b32_e32 v3, 7, v3
	v_lshlrev_b32_e32 v6, 4, v6
	s_movk_i32 s62, 0x70
	s_add_u32 s6, s80, s6
	v_and_b32_e32 v180, 31, v4
	v_and_or_b32 v188, v6, s62, v3
	v_bitop3_b32 v3, v5, v4, 15 bitop3:0x78
	s_addc_u32 s7, s81, s7
	s_load_dwordx2 s[16:17], s[8:9], 0x0
	s_load_dwordx2 s[18:19], s[6:7], 0x0
	v_lshlrev_b32_e32 v3, 4, v3
	v_lshlrev_b32_e32 v6, 7, v180
	s_movk_i32 s6, 0x4000
	v_and_b32_e32 v2, 63, v4
	v_lshl_or_b32 v189, v180, 8, v3
	v_or3_b32 v190, v3, v6, s6
	v_bfe_u32 v226, v4, 1, 3
	v_xor_b32_e32 v226, v226, v5
	v_lshlrev_b32_e32 v226, 4, v226
	v_or3_b32 v190, v226, v6, s6
	v_or_b32_e32 v189, 0x8000, v189
	v_or_b32_e32 v190, 0x8000, v190
	v_xor_b32_e32 v226, 32, v189
	v_xor_b32_e32 v227, 64, v189
	v_xor_b32_e32 v228, 0x60, v189
	v_xor_b32_e32 v232, 0x80, v189
	v_xor_b32_e32 v233, 0xa0, v189
	v_xor_b32_e32 v234, 0xc0, v189
	v_xor_b32_e32 v235, 0xe0, v189
	v_xor_b32_e32 v229, 32, v190
	v_xor_b32_e32 v230, 64, v190
	v_xor_b32_e32 v231, 0x60, v190
	v_lshlrev_b32_e32 v3, 4, v4
	v_lshlrev_b32_e32 v2, 3, v2
	v_and_b32_e32 v3, 0xc0, v3
	v_lshlrev_b32_e32 v6, 1, v4
	v_and_or_b32 v3, v2, 24, v3
	v_and_b32_e32 v6, 32, v6
	v_and_b32_e32 v2, 0x100, v2
	v_or3_b32 v2, v3, v6, v2
	v_add_u32_e32 v191, 0, v2
	v_mov_b32_e32 v3, 0
	v_lshlrev_b32_e32 v2, 4, v5
	v_lshlrev_b32_e32 v8, 3, v5
	v_lshl_add_u64 v[6:7], s[4:5], 0, v[2:3]
	s_mov_b64 s[4:5], 0x5e300000
	v_lshl_add_u64 v[182:183], v[6:7], 0, s[4:5]
	v_and_b32_e32 v2, 32, v4
	v_cvt_f32_ubyte0_e32 v4, v8
	v_or_b32_e32 v7, 1, v8
	s_waitcnt lgkmcnt(0)
; #define LAS __attribute__((address_space(3)))
; #define INF(i) ((const float*)arg_ptr(i))
; __device__ __forceinline__ int v_rd_base(int lane) { return ((lane & 3) << 3) | (((lane >> 2) & 3) << 6) | (((lane >> 4) & 1) << 5) | (((lane >> 5) & 1) << 8); }
; template <int layer>
; __device__ __forceinline__ void attn_phase(LAS unsigned char* lds) {
;     ...
;     const int tkp = (tid - 256) & 255; const unsigned kof0 = koff_n(tkp, 0), vof0 = voff_f(tkp, 0), rof0 = koff_r(tkp, 0);
;     const int kbn = r32 * 256 + ((hi * 16) ^ ((r32 & 7) << 4)), kbr0 = 16384 + r32 * 128 + ((hi * 16) ^ ((r32 & 7) << 4));
;     const unsigned ldsb = (unsigned)(uintptr_t)lds;
;     const int vb0 = (int)(unsigned)(uintptr_t)(lds + OFF_V) + v_rd_base(lane);
;     LAS float* wsl = (LAS float*)(lds + OFF_WS) + wid * 64; LAS float* li_l = wsl; LAS float* al_l = wsl + 32;
;     const float* cv_wgu = INF(layer == 0 ? 15 : 27); const float* cv_wdn = INF(layer == 0 ? 16 : 28); bf16* cv_gut = WSP(bf16, CV_MODE >= 2 ? WS_Q : WS_W_GUT); bf16* cv_dt = WSP(bf16, CV_MODE >= 2 ? WS_Q : WS_W_DT);
;     constexpr int CV_IG = 32 * 32, CV_ID = 8 * 64, CV_NIT = NEXP * (CV_IG + CV_ID);
;     int cv_it = (CV_MODE == 1) ? CV_NIT : bx * 4 + wid, cv_pend = -1; const int cv_stride = G * 4;
;     const unsigned cv_lds = (unsigned)(uintptr_t)(lds + OFF_CV) + (unsigned)(wid & 3) * 16384u;
;     ...
;                             for (int e = 0; e < 2; ++e) { const int j = 2 * jj + e; const int i = c * 16 + hi * 8 + j;
;                                 const float freq = exp2f(-(float)i * (13.287712379549449f / 32.0f)); float rev = pos * freq * 0.15915494309189535f; rev -= floorf(rev);
	v_lshl_add_u64 v[184:185], s[16:17], 0, v[2:3]
	v_mul_i32_i24_e32 v2, -4, v5
	v_mul_f32_e32 v5, 0xbed49a78, v4
	s_mov_b32 s6, 0xc2fc0000
	v_cvt_f32_ubyte0_e32 v7, v7
	v_mov_b32_e32 v6, 0x42800000
	v_cmp_gt_f32_e32 vcc, s6, v5
	v_mul_f32_e32 v9, 0xbed49a78, v7
	v_cmp_gt_f32_e64 s[4:5], s6, v9
	v_cndmask_b32_e32 v5, 0, v6, vcc
	v_fmac_f32_e32 v5, 0xbed49a78, v4
	v_cndmask_b32_e64 v9, 0, v6, s[4:5]
	v_exp_f32_e32 v4, v5
	v_fmac_f32_e32 v9, 0xbed49a78, v7
	v_exp_f32_e32 v7, v9
	v_not_b32_e32 v5, 63
	v_cndmask_b32_e32 v9, 0, v5, vcc
	v_ldexp_f32 v192, v4, v9
	v_cndmask_b32_e64 v4, 0, v5, s[4:5]
	v_ldexp_f32 v193, v7, v4
	v_or_b32_e32 v4, 2, v8
	v_cvt_f32_ubyte0_e32 v4, v4
	v_mul_f32_e32 v7, 0xbed49a78, v4
	v_cmp_gt_f32_e32 vcc, s6, v7
	s_lshl_b32 s7, s14, 5
	v_writelane_b32 v252, s18, 19
	v_cndmask_b32_e32 v7, 0, v6, vcc
	v_fmac_f32_e32 v7, 0xbed49a78, v4
	v_exp_f32_e32 v4, v7
	v_or_b32_e32 v7, 3, v8
	v_cvt_f32_ubyte0_e32 v7, v7
	v_mul_f32_e32 v9, 0xbed49a78, v7
	v_cmp_gt_f32_e64 s[4:5], s6, v9
	s_cmp_gt_i32 s14, 3
	v_writelane_b32 v252, s19, 20
	v_cndmask_b32_e64 v9, 0, v6, s[4:5]
	v_fmac_f32_e32 v9, 0xbed49a78, v7
	v_exp_f32_e32 v7, v9
	v_cndmask_b32_e32 v9, 0, v5, vcc
	v_ldexp_f32 v194, v4, v9
	v_cndmask_b32_e64 v4, 0, v5, s[4:5]
	v_ldexp_f32 v195, v7, v4
	v_or_b32_e32 v4, 4, v8
	v_cvt_f32_ubyte0_e32 v4, v4
	v_mul_f32_e32 v7, 0xbed49a78, v4
	v_cmp_gt_f32_e32 vcc, s6, v7
	s_cselect_b64 s[18:19], -1, 0
	s_lshl_b32 s64, s14, 10
	v_cndmask_b32_e32 v7, 0, v6, vcc
	v_fmac_f32_e32 v7, 0xbed49a78, v4
	v_exp_f32_e32 v4, v7
	v_or_b32_e32 v7, 5, v8
	v_cvt_f32_ubyte0_e32 v7, v7
	v_mul_f32_e32 v9, 0xbed49a78, v7
	v_cmp_gt_f32_e64 s[4:5], s6, v9
	s_add_i32 s64, s64, 0
	s_add_i32 s65, s64, 0x7000
	v_cndmask_b32_e64 v9, 0, v6, s[4:5]
	v_fmac_f32_e32 v9, 0xbed49a78, v7
	v_exp_f32_e32 v7, v9
	v_cndmask_b32_e32 v9, 0, v5, vcc
	v_ldexp_f32 v196, v4, v9
	v_cndmask_b32_e64 v4, 0, v5, s[4:5]
	v_ldexp_f32 v197, v7, v4
	v_or_b32_e32 v4, 6, v8
	v_cvt_f32_ubyte0_e32 v4, v4
	v_mul_f32_e32 v7, 0xbed49a78, v4
	v_cmp_gt_f32_e32 vcc, s6, v7
	s_add_i32 s66, s64, 0xb000
	s_add_i32 s67, s64, 0xfffff000
	v_cndmask_b32_e32 v7, 0, v6, vcc
	v_fmac_f32_e32 v7, 0xbed49a78, v4
	v_exp_f32_e32 v4, v7
	v_or_b32_e32 v7, 7, v8
	v_cvt_f32_ubyte0_e32 v7, v7
	v_mul_f32_e32 v9, 0xbed49a78, v7
	v_cmp_gt_f32_e64 s[4:5], s6, v9
	s_add_i32 s68, s64, 0xd000
	s_add_i32 s69, s64, 0x11000
	v_cndmask_b32_e64 v9, 0, v6, s[4:5]
	v_fmac_f32_e32 v9, 0xbed49a78, v7
	v_exp_f32_e32 v7, v9
	v_cndmask_b32_e32 v9, 0, v5, vcc
	v_ldexp_f32 v198, v4, v9
	v_cndmask_b32_e64 v4, 0, v5, s[4:5]
	v_ldexp_f32 v199, v7, v4
	v_or_b32_e32 v4, 16, v8
	v_cvt_f32_ubyte0_e32 v4, v4
	v_mul_f32_e32 v7, 0xbed49a78, v4
	v_cmp_gt_f32_e32 vcc, s6, v7
	s_add_i32 s70, s64, 0x3000
	v_writelane_b32 v252, s14, 21
	v_cndmask_b32_e32 v7, 0, v6, vcc
	v_fmac_f32_e32 v7, 0xbed49a78, v4
	v_exp_f32_e32 v4, v7
	v_or_b32_e32 v7, 17, v8
	v_cvt_f32_ubyte0_e32 v7, v7
	v_mul_f32_e32 v9, 0xbed49a78, v7
	v_cmp_gt_f32_e64 s[4:5], s6, v9
	s_cmp_lt_i32 s14, 4
	s_movk_i32 s61, 0x60
	v_cndmask_b32_e64 v9, 0, v6, s[4:5]
	v_fmac_f32_e32 v9, 0xbed49a78, v7
	v_exp_f32_e32 v7, v9
	v_cndmask_b32_e32 v9, 0, v5, vcc
	v_ldexp_f32 v200, v4, v9
	v_cndmask_b32_e64 v4, 0, v5, s[4:5]
	v_ldexp_f32 v201, v7, v4
	v_or_b32_e32 v4, 18, v8
	v_cvt_f32_ubyte0_e32 v4, v4
	v_mul_f32_e32 v7, 0xbed49a78, v4
	v_cmp_gt_f32_e32 vcc, s6, v7
	s_cselect_b64 s[20:21], -1, 0
	s_add_i32 s71, s24, 0x17000
	v_cndmask_b32_e32 v7, 0, v6, vcc
	v_fmac_f32_e32 v7, 0xbed49a78, v4
	v_exp_f32_e32 v4, v7
	v_or_b32_e32 v7, 19, v8
	v_cvt_f32_ubyte0_e32 v7, v7
	v_mul_f32_e32 v9, 0xbed49a78, v7
	v_cmp_gt_f32_e64 s[4:5], s6, v9
	s_mov_b32 s72, 0x42800000
	v_or_b32_e32 v208, 0x20000, v1
	v_cndmask_b32_e64 v9, 0, v6, s[4:5]
	v_fmac_f32_e32 v9, 0xbed49a78, v7
	v_exp_f32_e32 v7, v9
	v_cndmask_b32_e32 v9, 0, v5, vcc
	v_ldexp_f32 v202, v4, v9
	v_cndmask_b32_e64 v4, 0, v5, s[4:5]
	v_ldexp_f32 v203, v7, v4
	v_or_b32_e32 v4, 20, v8
	v_cvt_f32_ubyte0_e32 v4, v4
	v_mul_f32_e32 v7, 0xbed49a78, v4
	v_cmp_gt_f32_e32 vcc, s6, v7
	s_add_i32 s73, s64, 0x8000
	v_or_b32_e32 v209, 0x40000, v1
	v_cndmask_b32_e32 v7, 0, v6, vcc
	v_fmac_f32_e32 v7, 0xbed49a78, v4
	v_exp_f32_e32 v4, v7
	v_or_b32_e32 v7, 21, v8
	v_cvt_f32_ubyte0_e32 v7, v7
	v_mul_f32_e32 v9, 0xbed49a78, v7
	v_cmp_gt_f32_e64 s[4:5], s6, v9
	s_add_i32 s74, s64, 0x9000
	v_or_b32_e32 v210, 0x60000, v1
	v_cndmask_b32_e64 v9, 0, v6, s[4:5]
	v_fmac_f32_e32 v9, 0xbed49a78, v7
	v_exp_f32_e32 v7, v9
	v_cndmask_b32_e32 v9, 0, v5, vcc
	v_ldexp_f32 v204, v4, v9
	v_cndmask_b32_e64 v4, 0, v5, s[4:5]
	v_ldexp_f32 v205, v7, v4
	v_or_b32_e32 v4, 22, v8
	v_cvt_f32_ubyte0_e32 v4, v4
	v_mul_f32_e32 v7, 0xbed49a78, v4
	v_cmp_gt_f32_e32 vcc, s6, v7
	s_add_i32 s75, s64, 0xa000
	v_or_b32_e32 v211, 0x1000, v188
	v_cndmask_b32_e32 v7, 0, v6, vcc
	v_fmac_f32_e32 v7, 0xbed49a78, v4
	v_exp_f32_e32 v4, v7
	v_or_b32_e32 v7, 23, v8
	v_cvt_f32_ubyte0_e32 v7, v7
	v_mul_f32_e32 v8, 0xbed49a78, v7
	v_cmp_gt_f32_e64 s[4:5], s6, v8
	s_add_i32 s76, s64, 0xc000
	v_or_b32_e32 v212, 0x20000, v181
	v_cndmask_b32_e64 v6, 0, v6, s[4:5]
	v_fmac_f32_e32 v6, 0xbed49a78, v7
	v_exp_f32_e32 v6, v6
	v_cndmask_b32_e32 v7, 0, v5, vcc
	v_ldexp_f32 v206, v4, v7
	v_cndmask_b32_e64 v4, 0, v5, s[4:5]
	v_ldexp_f32 v207, v6, v4
	v_or_b32_e32 v213, 0x40000, v181
	s_add_i32 s77, s64, 0x1000
	v_or_b32_e32 v214, 0x60000, v181
	s_add_i32 s78, s64, 0x2000
	s_add_i32 s79, s64, 0xe000
	s_add_i32 s80, s64, 0xf000
	s_add_i32 s81, s64, 0x10000
	s_add_i32 s82, s64, 0x12000
	s_add_i32 s83, s64, 0x4000
	s_add_i32 s84, s64, 0x5000
	s_add_i32 s85, s64, 0x6000
	s_add_i32 s86, s24, 0x15400
	s_add_i32 s87, s24, 0x15800
	s_add_i32 s88, s24, 0x15c00
	s_add_i32 s89, s24, 0x16000
	s_add_i32 s90, s24, 0x16400
	s_add_i32 s91, s24, 0x16800
	s_add_i32 s92, s24, 0x16c00
	s_add_i32 s93, s24, 0x17400
	s_add_i32 s94, s24, 0x17800
	s_add_i32 s95, s24, 0x17c00
	s_add_i32 s96, s24, 0x18000
	s_add_i32 s97, s24, 0x18400
	s_add_i32 s27, s24, 0x18800
	v_writelane_b32 v252, s24, 22
	s_add_i32 s26, s24, 0x18c00
	v_add3_u32 v215, v2, s7, v180
	v_mov_b32_e32 v216, 0x358637bd
	s_movk_i32 s30, 0x3ff
	s_movk_i32 s31, 0x50
	v_mov_b32_e32 v217, 0x1800
	v_mov_b32_e32 v218, 0x10000
	v_mov_b32_e32 v219, 0xff800000
	v_writelane_b32 v252, s7, 23

.LBB0_538:
	v_cndmask_b32_e64 v2, 0, 1, s[20:21]
	v_cmp_ne_u32_e64 s[6:7], 1, v2
	s_andn2_b64 vcc, exec, s[20:21]
	s_cmp_lt_i32 s33, 0
	s_cbranch_scc0 .LBB0_550
	s_cmp_gt_i32 s15, 0x17fff
	s_cbranch_scc1 .LBB0_551
.LBB0_541:
	s_and_b64 vcc, exec, s[20:21]
	s_add_i32 s33, s15, 0xffff0000
	s_cmp_lt_i32 s15, 0x10000
	s_cselect_b32 s33, s15, s33
	s_cselect_b32 s41, s30, 0x1ff
	s_cselect_b32 s42, 10, 11
	s_cselect_b32 s40, 10, 9
	s_cselect_b32 s43, s11, s13
	s_cselect_b32 s44, s10, s12
	s_cselect_b32 s45, 21, 20
	s_and_b32 s41, s33, s41
	s_add_i32 s56, s42, -5
	s_lshr_b32 s41, s41, s56
	s_ashr_i32 s40, s33, s40
	s_lshl_b32 s57, s41, 6
	s_lshl_b32 s41, -1, s56
	s_andn2_b32 s33, s33, s41
	s_ashr_i32 s41, s40, 31
	s_lshl_b64 s[40:41], s[40:41], s45
	s_lshl_b64 s[40:41], s[40:41], 2
	s_add_u32 s40, s44, s40
	s_addc_u32 s41, s43, s41
	s_lshl_b32 s43, s57, s42
	v_mov_b32_e32 v2, v0
	s_lshl_b32 s43, s43, 2
	s_add_u32 s40, s40, s43
	v_bfe_u32 v68, v2, 3, 3
	v_lshlrev_b32_e32 v68, s42, v68
	s_addc_u32 s41, s41, 0
	s_lshl_b32 s33, s33, 7
	v_lshlrev_b32_e32 v2, 4, v2
	v_lshlrev_b32_e32 v68, 2, v68
	s_add_u32 s40, s40, s33
	v_and_b32_e32 v69, 0x70, v2
	s_addc_u32 s41, s41, 0
	v_or_b32_e32 v70, v68, v69
	s_cbranch_vccnz .Lcvs_a0b0_0
	s_mov_b32 s33, m0
	s_mov_b32 m0, s23
	s_nop 0
	global_load_lds_dwordx4 v70, s[40:41] nt
	s_mov_b32 m0, s33
.Lcvs_a0b0_0:
	s_lshl_b32 s33, 32, s42
	s_add_u32 s56, s40, s33
	s_addc_u32 s57, s41, 0
	v_bitop3_b32 v70, v68, 16, v69 bitop3:0x36
	s_cbranch_vccnz .Lcvs_a0b0_1
	s_mov_b32 s33, m0
	s_mov_b32 m0, s86
	s_nop 0
	global_load_lds_dwordx4 v70, s[56:57] nt
	s_mov_b32 m0, s33
.Lcvs_a0b0_1:
	s_lshl_b32 s33, 64, s42
	s_add_u32 s56, s40, s33
	s_addc_u32 s57, s41, 0
	v_bitop3_b32 v70, v68, 32, v69 bitop3:0x36
	s_cbranch_vccnz .Lcvs_a0b0_2
	s_mov_b32 s33, m0
	s_mov_b32 m0, s87
	s_nop 0
	global_load_lds_dwordx4 v70, s[56:57] nt
	s_mov_b32 m0, s33
.Lcvs_a0b0_2:
	s_lshl_b32 s33, 0x60, s42
	s_add_u32 s56, s40, s33
	s_addc_u32 s57, s41, 0
	v_bitop3_b32 v70, v68, 48, v69 bitop3:0x36
	s_cbranch_vccnz .Lcvs_a0b0_3
	s_mov_b32 s33, m0
	s_mov_b32 m0, s88
	s_nop 0
	global_load_lds_dwordx4 v70, s[56:57] nt
	s_mov_b32 m0, s33
.Lcvs_a0b0_3:
	s_lshl_b32 s33, 0x80, s42
	s_add_u32 s56, s40, s33
	s_addc_u32 s57, s41, 0
	v_bitop3_b32 v70, v68, 64, v69 bitop3:0x36
	s_cbranch_vccnz .Lcvs_a0b0_4
	s_mov_b32 s33, m0
	s_mov_b32 m0, s89
	s_nop 0
	global_load_lds_dwordx4 v70, s[56:57] nt
	s_mov_b32 m0, s33
.Lcvs_a0b0_4:
	s_lshl_b32 s33, 0xa0, s42
	s_add_u32 s56, s40, s33
	s_addc_u32 s57, s41, 0
	v_bitop3_b32 v70, v68, s31, v69 bitop3:0x36
	s_cbranch_vccnz .Lcvs_a0b0_5
	s_mov_b32 s33, m0
	s_mov_b32 m0, s90
	s_nop 0
	global_load_lds_dwordx4 v70, s[56:57] nt
	s_mov_b32 m0, s33
.Lcvs_a0b0_5:
	s_lshl_b32 s33, 0xc0, s42
	s_add_u32 s56, s40, s33
	s_addc_u32 s57, s41, 0
	v_bitop3_b32 v69, v68, s61, v69 bitop3:0x36
	s_cbranch_vccnz .Lcvs_a0b0_6
	s_mov_b32 s33, m0
	s_mov_b32 m0, s91
	s_nop 0
	global_load_lds_dwordx4 v69, s[56:57] nt
	s_mov_b32 m0, s33
.Lcvs_a0b0_6:
	s_lshl_b32 s33, 0xe0, s42
	s_add_u32 s40, s40, s33
	s_addc_u32 s41, s41, 0
	v_bitop3_b32 v2, v68, s62, v2 bitop3:0x34
	s_cbranch_vccnz .Lcvs_a0b0_7
	s_mov_b32 s33, m0
	s_mov_b32 m0, s92
	s_nop 0
	global_load_lds_dwordx4 v2, s[40:41] nt
	s_mov_b32 m0, s33
.Lcvs_a0b0_7:
	s_add_i32 s59, s15, s22
	s_mov_b32 s33, s15
	s_sub_i32 s15, s63, 63
	s_cmp_gt_i32 s15, s16
	s_cbranch_scc0 .LBB0_552

.LBB0_546:
	s_and_b64 vcc, exec, s[6:7]
	s_cmp_lt_i32 s33, 0
	s_cbranch_scc0 .LBB0_565
	s_cmp_gt_i32 s59, 0x17fff
	s_cbranch_scc1 .LBB0_566
.LBB0_549:
	s_and_b64 vcc, exec, s[20:21]
	s_add_i32 s6, s59, 0xffff0000
	s_cmp_lt_i32 s59, 0x10000
	s_cselect_b32 s7, s59, s6
	s_cselect_b32 s15, s30, 0x1ff
	s_cselect_b32 s33, 10, 11
	s_cselect_b32 s6, 10, 9
	s_cselect_b32 s40, s11, s13
	s_cselect_b32 s41, s10, s12
	s_cselect_b32 s42, 21, 20
	s_and_b32 s15, s7, s15
	s_add_i32 s43, s33, -5
	s_ashr_i32 s6, s7, s6
	s_lshr_b32 s15, s15, s43
	s_lshl_b32 s43, -1, s43
	s_andn2_b32 s43, s7, s43
	s_ashr_i32 s7, s6, 31
	s_lshl_b64 s[6:7], s[6:7], s42
	s_lshl_b32 s15, s15, 6
	s_lshl_b64 s[6:7], s[6:7], 2
	s_add_u32 s6, s41, s6
	s_addc_u32 s7, s40, s7
	s_lshl_b32 s15, s15, s33
	v_mov_b32_e32 v2, v0
	s_lshl_b32 s15, s15, 2
	s_add_u32 s6, s6, s15
	v_bfe_u32 v68, v2, 3, 3
	v_lshlrev_b32_e32 v68, s33, v68
	s_addc_u32 s7, s7, 0
	s_lshl_b32 s15, s43, 7
	v_lshlrev_b32_e32 v2, 4, v2
	v_lshlrev_b32_e32 v68, 2, v68
	s_add_u32 s6, s6, s15
	v_and_b32_e32 v69, 0x70, v2
	s_addc_u32 s7, s7, 0
	v_or_b32_e32 v70, v68, v69
	s_cbranch_vccnz .Lcvs_a0b1_0
	s_mov_b32 s15, m0
	s_mov_b32 m0, s71
	s_nop 0
	global_load_lds_dwordx4 v70, s[6:7] nt
	s_mov_b32 m0, s15
.Lcvs_a0b1_0:
	s_lshl_b32 s15, 32, s33
	s_add_u32 s40, s6, s15
	s_addc_u32 s41, s7, 0
	v_bitop3_b32 v70, v68, 16, v69 bitop3:0x36
	s_cbranch_vccnz .Lcvs_a0b1_1
	s_mov_b32 s15, m0
	s_mov_b32 m0, s93
	s_nop 0
	global_load_lds_dwordx4 v70, s[40:41] nt
	s_mov_b32 m0, s15
.Lcvs_a0b1_1:
	s_lshl_b32 s15, 64, s33
	s_add_u32 s40, s6, s15
	s_addc_u32 s41, s7, 0
	v_bitop3_b32 v70, v68, 32, v69 bitop3:0x36
	s_cbranch_vccnz .Lcvs_a0b1_2
	s_mov_b32 s15, m0
	s_mov_b32 m0, s94
	s_nop 0
	global_load_lds_dwordx4 v70, s[40:41] nt
	s_mov_b32 m0, s15
.Lcvs_a0b1_2:
	s_lshl_b32 s15, 0x60, s33
	s_add_u32 s40, s6, s15
	s_addc_u32 s41, s7, 0
	v_bitop3_b32 v70, v68, 48, v69 bitop3:0x36
	s_cbranch_vccnz .Lcvs_a0b1_3
	s_mov_b32 s15, m0
	s_mov_b32 m0, s95
	s_nop 0
	global_load_lds_dwordx4 v70, s[40:41] nt
	s_mov_b32 m0, s15
.Lcvs_a0b1_3:
	s_lshl_b32 s15, 0x80, s33
	s_add_u32 s40, s6, s15
	s_addc_u32 s41, s7, 0
	v_bitop3_b32 v70, v68, 64, v69 bitop3:0x36
	s_cbranch_vccnz .Lcvs_a0b1_4
	s_mov_b32 s15, m0
	s_mov_b32 m0, s96
	s_nop 0
	global_load_lds_dwordx4 v70, s[40:41] nt
	s_mov_b32 m0, s15
.Lcvs_a0b1_4:
	s_lshl_b32 s15, 0xa0, s33
	s_add_u32 s40, s6, s15
	s_addc_u32 s41, s7, 0
	v_bitop3_b32 v70, v68, s31, v69 bitop3:0x36
	s_cbranch_vccnz .Lcvs_a0b1_5
	s_mov_b32 s15, m0
	s_mov_b32 m0, s97
	s_nop 0
	global_load_lds_dwordx4 v70, s[40:41] nt
	s_mov_b32 m0, s15
.Lcvs_a0b1_5:
	s_lshl_b32 s15, 0xc0, s33
	s_add_u32 s40, s6, s15
	s_addc_u32 s41, s7, 0
	v_bitop3_b32 v69, v68, s61, v69 bitop3:0x36
	s_cbranch_vccnz .Lcvs_a0b1_6
	s_mov_b32 s15, m0
	s_mov_b32 m0, s27
	s_nop 0
	global_load_lds_dwordx4 v69, s[40:41] nt
	s_mov_b32 m0, s15
.Lcvs_a0b1_6:
	s_lshl_b32 s15, 0xe0, s33
	s_add_u32 s6, s6, s15
	s_addc_u32 s7, s7, 0
	v_bitop3_b32 v2, v68, s62, v2 bitop3:0x34
	s_cbranch_vccnz .Lcvs_a0b1_7
	s_mov_b32 s15, m0
	s_mov_b32 m0, s26
	s_nop 0
	global_load_lds_dwordx4 v2, s[6:7] nt
	s_mov_b32 m0, s15
.Lcvs_a0b1_7:
	s_add_i32 s15, s59, s22
	s_mov_b32 s33, s59
	s_add_i32 s6, s63, 1
	s_cmp_gt_i32 s6, s16
	s_cbranch_scc1 .LBB0_532
	s_branch .LBB0_567
.Lfsk_a0b0:
	s_mov_b32 s33, -1
	s_cmp_gt_i32 s15, 0x17fff
	s_cbranch_scc0 .LBB0_541
	s_branch .LBB0_551
.LBB0_550:
	s_and_b64 vcc, exec, s[18:19]
	s_cbranch_vccnz .Lfsk_a0b0
	v_sub_co_u32_e32 v2, vcc, s33, v218
	s_and_b64 s[56:57], vcc, exec
	v_readfirstlane_b32 s40, v2
	s_cselect_b32 s40, s33, s40
	s_cselect_b32 s56, s30, 0x1ff
	s_cselect_b32 s41, 10, 9
	s_and_b32 s59, s40, s56
	v_mov_b32_e32 v102, v0
	s_waitcnt vmcnt(0)
	s_and_b64 s[56:57], vcc, exec
	s_cselect_b32 s56, 5, 6
	v_and_b32_e32 v2, 7, v102
	v_lshrrev_b32_e32 v68, 3, v102
	v_bfe_u32 v100, v102, 3, 2
	v_lshlrev_b32_e32 v69, 10, v2
	v_lshlrev_b32_e32 v70, 2, v2
	v_and_b32_e32 v71, 4, v68
	v_lshlrev_b32_e32 v72, 2, v100
	s_lshr_b32 s59, s59, s56
	s_lshl_b32 s56, -1, s56
	v_add3_u32 v69, s23, v69, v72
	v_bitop3_b32 v72, v71, v70, 8 bitop3:0x36
	s_andn2_b32 s42, s40, s56
	v_bitop3_b32 v68, v68, v70, 4 bitop3:0x6c
	v_lshl_add_u32 v76, v72, 2, v69
	v_bitop3_b32 v72, v71, v70, 16 bitop3:0x36
	v_bitop3_b32 v70, v71, v70, 24 bitop3:0x36
	s_lshl_b32 s43, s42, 5
	v_lshl_add_u32 v68, v68, 2, v69
	v_lshl_add_u32 v84, v72, 2, v69
	v_lshl_add_u32 v92, v70, 2, v69
	s_and_b64 s[56:57], vcc, exec
	v_add_u32_e32 v74, 0x2000, v68
	v_add_u32_e32 v82, 0x2000, v76
	v_add_u32_e32 v90, 0x2000, v84
	v_add_u32_e32 v98, 0x2000, v92
	s_cselect_b32 s44, s1, s3
	s_cselect_b32 s45, s0, s2
	s_ashr_i32 s56, s40, s41
	ds_read2_b32 v[68:69], v74 offset1:32
	ds_read2_b32 v[70:71], v74 offset0:64 offset1:96
	ds_read2_b32 v[72:73], v74 offset0:128 offset1:160
	ds_read2_b32 v[74:75], v74 offset0:192 offset1:224
	ds_read2_b32 v[76:77], v82 offset1:32
	ds_read2_b32 v[78:79], v82 offset0:64 offset1:96
	ds_read2_b32 v[80:81], v82 offset0:128 offset1:160
	ds_read2_b32 v[82:83], v82 offset0:192 offset1:224
	ds_read2_b32 v[84:85], v90 offset1:32
	ds_read2_b32 v[86:87], v90 offset0:64 offset1:96
	ds_read2_b32 v[88:89], v90 offset0:128 offset1:160
	ds_read2_b32 v[90:91], v90 offset0:192 offset1:224
	ds_read2_b32 v[92:93], v98 offset1:32
	ds_read2_b32 v[94:95], v98 offset0:64 offset1:96
	ds_read2_b32 v[96:97], v98 offset0:128 offset1:160
	ds_read2_b32 v[98:99], v98 offset0:192 offset1:224
	s_ashr_i32 s57, s56, 31
	s_and_b64 s[40:41], vcc, exec
	s_cselect_b32 s40, 21, 20
	s_lshl_b64 s[40:41], s[56:57], s40
	s_waitcnt lgkmcnt(0)
	s_lshl_b64 s[40:41], s[40:41], 1
	s_add_u32 s40, s45, s40
	v_bfe_u32 v103, v102, 3, 3
	s_addc_u32 s41, s44, s41
	s_lshl_b32 s44, s42, 6
	s_lshl_b32 s33, s33, 6
	s_and_b32 s45, s44, 0x300
	s_and_b32 s33, s33, 0x80
	s_lshr_b32 s42, s42, 2
	s_or_b32 s33, s45, s33
	s_and_b32 s42, s42, 28
	s_or_b32 s33, s33, s42
	v_or_b32_e32 v104, s33, v100
	s_lshl_b32 s33, s59, 7
	s_add_u32 s40, s40, s33
	s_addc_u32 s41, s41, 0
	v_lshlrev_b32_e32 v2, 4, v2
	v_lshl_add_u64 v[100:101], s[40:41], 0, v[2:3]
	v_lshrrev_b32_e32 v2, 2, v102
	v_and_b32_e32 v2, 8, v2
	s_waitcnt lgkmcnt(14)
	v_cvt_pk_bf16_f32 v68, v68, v69
	v_cvt_pk_bf16_f32 v69, v70, v71
	s_waitcnt lgkmcnt(12)
	v_cvt_pk_bf16_f32 v71, v74, v75
	s_and_b32 s33, s44, 64
	v_add_u32_e32 v75, v104, v2
	v_or_b32_e32 v74, s43, v103
	v_or_b32_e32 v2, s33, v75
	s_and_b64 s[40:41], vcc, exec
	v_cndmask_b32_e32 v2, v74, v2, vcc
	s_cselect_b32 s40, 11, 9
	v_cvt_pk_bf16_f32 v70, v72, v73
	v_lshlrev_b64 v[72:73], s40, v[2:3]
	v_lshl_add_u64 v[72:73], v[72:73], 1, v[100:101]
	v_or_b32_e32 v2, 8, v103
	global_store_dwordx4 v[72:73], v[68:71], off nt
	v_or_b32_e32 v72, s43, v2
	v_lshlrev_b32_e32 v2, 1, v2
	v_and_b32_e32 v2, 24, v2
	v_add_u32_e32 v2, v2, v104
	v_or_b32_e32 v2, s33, v2
	v_cndmask_b32_e32 v2, v72, v2, vcc
	v_lshlrev_b64 v[72:73], s40, v[2:3]
	v_lshl_add_u64 v[72:73], v[72:73], 1, v[100:101]
	v_or_b32_e32 v2, 16, v74
	s_waitcnt lgkmcnt(11)
	v_cvt_pk_bf16_f32 v68, v76, v77
	s_waitcnt lgkmcnt(10)
	v_cvt_pk_bf16_f32 v69, v78, v79
	s_waitcnt lgkmcnt(9)
	v_cvt_pk_bf16_f32 v70, v80, v81
	s_waitcnt lgkmcnt(8)
	v_cvt_pk_bf16_f32 v71, v82, v83
	global_store_dwordx4 v[72:73], v[68:71], off nt
	v_lshlrev_b32_e32 v72, 1, v2
	v_and_b32_e32 v72, 0x60, v72
	v_add_u32_e32 v72, v75, v72
	v_cndmask_b32_e32 v2, v2, v72, vcc
	v_lshlrev_b64 v[72:73], s40, v[2:3]
	v_lshl_add_u64 v[72:73], v[72:73], 1, v[100:101]
	v_or_b32_e32 v2, 24, v103
	s_waitcnt lgkmcnt(7)
	v_cvt_pk_bf16_f32 v68, v84, v85
	s_waitcnt lgkmcnt(6)
	v_cvt_pk_bf16_f32 v69, v86, v87
	s_waitcnt lgkmcnt(5)
	v_cvt_pk_bf16_f32 v70, v88, v89
	s_waitcnt lgkmcnt(4)
	v_cvt_pk_bf16_f32 v71, v90, v91
	global_store_dwordx4 v[72:73], v[68:71], off nt
	v_or_b32_e32 v72, s43, v2
	v_lshlrev_b32_e32 v73, 1, v72
	v_lshlrev_b32_e32 v2, 1, v2
	v_and_b32_e32 v73, 0x60, v73
	v_and_b32_e32 v2, 24, v2
	v_add3_u32 v2, v2, v104, v73
	v_cndmask_b32_e32 v2, v72, v2, vcc
	v_lshlrev_b64 v[72:73], s40, v[2:3]
	v_lshl_add_u64 v[72:73], v[72:73], 1, v[100:101]
	s_mov_b32 s33, -1
	s_waitcnt lgkmcnt(3)
	v_cvt_pk_bf16_f32 v68, v92, v93
	s_waitcnt lgkmcnt(2)
	v_cvt_pk_bf16_f32 v69, v94, v95
	s_waitcnt lgkmcnt(1)
	v_cvt_pk_bf16_f32 v70, v96, v97
	s_waitcnt lgkmcnt(0)
	v_cvt_pk_bf16_f32 v71, v98, v99
	global_store_dwordx4 v[72:73], v[68:71], off nt
	s_cmp_gt_i32 s15, 0x17fff
	s_cbranch_scc0 .LBB0_541

.Lfsk_a0b1:
	s_mov_b32 s33, -1
	s_cmp_gt_i32 s59, 0x17fff
	s_cbranch_scc0 .LBB0_549
	s_branch .LBB0_566
.LBB0_565:
	s_and_b64 vcc, exec, s[18:19]
	s_cbranch_vccnz .Lfsk_a0b1
	v_sub_co_u32_e32 v2, vcc, s33, v218
	s_and_b64 s[6:7], vcc, exec
	v_mov_b32_e32 v102, v0
	s_waitcnt vmcnt(0)
	v_readfirstlane_b32 s6, v2
	s_cselect_b32 s15, s33, s6
	v_and_b32_e32 v2, 7, v102
	v_bfe_u32 v100, v102, 3, 2
	v_lshrrev_b32_e32 v68, 3, v102
	v_lshlrev_b32_e32 v69, 10, v2
	v_lshlrev_b32_e32 v70, 2, v2
	v_lshlrev_b32_e32 v72, 2, v100
	v_and_b32_e32 v71, 4, v68
	v_add3_u32 v69, s23, v69, v72
	v_bitop3_b32 v68, v68, v70, 4 bitop3:0x6c
	v_lshl_add_u32 v74, v68, 2, v69
	v_bitop3_b32 v68, v71, v70, 8 bitop3:0x36
	v_lshl_add_u32 v82, v68, 2, v69
	v_bitop3_b32 v68, v71, v70, 16 bitop3:0x36
	v_lshl_add_u32 v90, v68, 2, v69
	v_bitop3_b32 v68, v71, v70, 24 bitop3:0x36
	v_lshl_add_u32 v98, v68, 2, v69
	ds_read2_b32 v[68:69], v74 offset1:32
	ds_read2_b32 v[70:71], v74 offset0:64 offset1:96
	ds_read2_b32 v[72:73], v74 offset0:128 offset1:160
	ds_read2_b32 v[74:75], v74 offset0:192 offset1:224
	ds_read2_b32 v[76:77], v82 offset1:32
	ds_read2_b32 v[78:79], v82 offset0:64 offset1:96
	ds_read2_b32 v[80:81], v82 offset0:128 offset1:160
	ds_read2_b32 v[82:83], v82 offset0:192 offset1:224
	ds_read2_b32 v[84:85], v90 offset1:32
	ds_read2_b32 v[86:87], v90 offset0:64 offset1:96
	ds_read2_b32 v[88:89], v90 offset0:128 offset1:160
	ds_read2_b32 v[90:91], v90 offset0:192 offset1:224
	ds_read2_b32 v[92:93], v98 offset1:32
	ds_read2_b32 v[94:95], v98 offset0:64 offset1:96
	ds_read2_b32 v[96:97], v98 offset0:128 offset1:160
	ds_read2_b32 v[98:99], v98 offset0:192 offset1:224
	s_cselect_b32 s6, s30, 0x1ff
	s_cselect_b32 s40, 10, 9
	s_and_b32 s41, s15, s6
	s_and_b64 s[6:7], vcc, exec
	s_cselect_b32 s6, 5, 6
	s_lshr_b32 s42, s41, s6
	s_lshl_b32 s6, -1, s6
	s_andn2_b32 s43, s15, s6
	s_lshl_b32 s44, s43, 5
	s_and_b64 s[6:7], vcc, exec
	s_cselect_b32 s45, s1, s3
	s_cselect_b32 s56, s0, s2
	s_ashr_i32 s6, s15, s40
	s_ashr_i32 s7, s6, 31
	s_and_b64 s[40:41], vcc, exec
	s_cselect_b32 s15, 21, 20
	s_lshl_b64 s[6:7], s[6:7], s15
	s_waitcnt lgkmcnt(0)
	s_lshl_b64 s[6:7], s[6:7], 1
	s_add_u32 s6, s56, s6
	v_bfe_u32 v103, v102, 3, 3
	s_addc_u32 s7, s45, s7
	s_lshl_b32 s15, s43, 6
	s_lshl_b32 s33, s33, 6
	s_and_b32 s40, s15, 0x300
	s_and_b32 s33, s33, 0x80
	s_or_b32 s33, s40, s33
	s_lshr_b32 s40, s43, 2
	s_and_b32 s40, s40, 28
	s_or_b32 s33, s33, s40
	v_or_b32_e32 v104, s33, v100
	s_lshl_b32 s33, s42, 7
	s_add_u32 s6, s6, s33
	s_addc_u32 s7, s7, 0
	v_lshlrev_b32_e32 v2, 4, v2
	v_lshl_add_u64 v[100:101], s[6:7], 0, v[2:3]
	v_lshrrev_b32_e32 v2, 2, v102
	v_and_b32_e32 v2, 8, v2
	s_waitcnt lgkmcnt(14)
	v_cvt_pk_bf16_f32 v68, v68, v69
	v_cvt_pk_bf16_f32 v69, v70, v71
	s_waitcnt lgkmcnt(12)
	v_cvt_pk_bf16_f32 v71, v74, v75
	s_and_b32 s15, s15, 64
	v_add_u32_e32 v75, v104, v2
	v_or_b32_e32 v74, s44, v103
	v_or_b32_e32 v2, s15, v75
	s_and_b64 s[6:7], vcc, exec
	v_cndmask_b32_e32 v2, v74, v2, vcc
	s_cselect_b32 s6, 11, 9
	v_cvt_pk_bf16_f32 v70, v72, v73
	v_lshlrev_b64 v[72:73], s6, v[2:3]
	v_lshl_add_u64 v[72:73], v[72:73], 1, v[100:101]
	v_or_b32_e32 v2, 8, v103
	global_store_dwordx4 v[72:73], v[68:71], off nt
	v_or_b32_e32 v72, s44, v2
	v_lshlrev_b32_e32 v2, 1, v2
	v_and_b32_e32 v2, 24, v2
	v_add_u32_e32 v2, v2, v104
	v_or_b32_e32 v2, s15, v2
	v_cndmask_b32_e32 v2, v72, v2, vcc
	v_lshlrev_b64 v[72:73], s6, v[2:3]
	v_lshl_add_u64 v[72:73], v[72:73], 1, v[100:101]
	v_or_b32_e32 v2, 16, v74
	s_waitcnt lgkmcnt(11)
	v_cvt_pk_bf16_f32 v68, v76, v77
	s_waitcnt lgkmcnt(10)
	v_cvt_pk_bf16_f32 v69, v78, v79
	s_waitcnt lgkmcnt(9)
	v_cvt_pk_bf16_f32 v70, v80, v81
	s_waitcnt lgkmcnt(8)
	v_cvt_pk_bf16_f32 v71, v82, v83
	global_store_dwordx4 v[72:73], v[68:71], off nt
	v_lshlrev_b32_e32 v72, 1, v2
	v_and_b32_e32 v72, 0x60, v72
	v_add_u32_e32 v72, v75, v72
	v_cndmask_b32_e32 v2, v2, v72, vcc
	v_lshlrev_b64 v[72:73], s6, v[2:3]
	v_lshl_add_u64 v[72:73], v[72:73], 1, v[100:101]
	v_or_b32_e32 v2, 24, v103
	s_waitcnt lgkmcnt(7)
	v_cvt_pk_bf16_f32 v68, v84, v85
	s_waitcnt lgkmcnt(6)
	v_cvt_pk_bf16_f32 v69, v86, v87
	s_waitcnt lgkmcnt(5)
	v_cvt_pk_bf16_f32 v70, v88, v89
	s_waitcnt lgkmcnt(4)
	v_cvt_pk_bf16_f32 v71, v90, v91
	global_store_dwordx4 v[72:73], v[68:71], off nt
	v_or_b32_e32 v72, s44, v2
	v_lshlrev_b32_e32 v73, 1, v72
	v_lshlrev_b32_e32 v2, 1, v2
	v_and_b32_e32 v73, 0x60, v73
	v_and_b32_e32 v2, 24, v2
	v_add3_u32 v2, v2, v104, v73
	v_cndmask_b32_e32 v2, v72, v2, vcc
	v_lshlrev_b64 v[72:73], s6, v[2:3]
	v_lshl_add_u64 v[72:73], v[72:73], 1, v[100:101]
	s_mov_b32 s33, -1
	s_waitcnt lgkmcnt(3)
	v_cvt_pk_bf16_f32 v68, v92, v93
	s_waitcnt lgkmcnt(2)
	v_cvt_pk_bf16_f32 v69, v94, v95
	s_waitcnt lgkmcnt(1)
	v_cvt_pk_bf16_f32 v70, v96, v97
	s_waitcnt lgkmcnt(0)
	v_cvt_pk_bf16_f32 v71, v98, v99
	global_store_dwordx4 v[72:73], v[68:71], off nt
	s_cmp_gt_i32 s59, 0x17fff
	s_cbranch_scc0 .LBB0_549

; #define LAS __attribute__((address_space(3)))
; #define INF(i) ((const float*)arg_ptr(i))
; __device__ __forceinline__ int v_rd_base(int lane) { return ((lane & 3) << 3) | (((lane >> 2) & 3) << 6) | (((lane >> 4) & 1) << 5) | (((lane >> 5) & 1) << 8); }
; template <int layer>
; __device__ __forceinline__ void attn_phase(LAS unsigned char* lds) {
;     ...
;     const int wid = __builtin_amdgcn_readfirstlane(tid >> 6), r32 = lane & 31, hi = lane >> 5;
;     auto koff_n = [](int tk, int j) { const int ci = j * 256 + tk, row = ci >> 4, pc = ci & 15, lc = pc ^ (row & 7); return (unsigned)(row * KLD + lc * 8) * 2u; };
;     auto koff_r = [](int tk, int j) { const int ci = j * 256 + tk, row = ci >> 3, pc = ci & 7, lc = pc ^ (row & 7); return (unsigned)(row * 64 + lc * 8) * 2u; };
;     auto voff_f = [](int tk, int j) { const int ci = j * 256 + tk, st = ci >> 5, w = ci & 31, kk = (st >> 2) * 8 + (w >> 2), key = (kk & ~0xC) | ((kk & 4) << 1) | ((kk & 8) >> 1), c = (st & 3) * 32 + (w & 3) * 8;
;         return (unsigned)(key * KLD + c) * 2u; };
;     const int tkp = (tid - 256) & 255; const unsigned kof0 = koff_n(tkp, 0), vof0 = voff_f(tkp, 0), rof0 = koff_r(tkp, 0);
;     const int kbn = r32 * 256 + ((hi * 16) ^ ((r32 & 7) << 4)), kbr0 = 16384 + r32 * 128 + ((hi * 16) ^ ((r32 & 7) << 4));
;     const unsigned ldsb = (unsigned)(uintptr_t)lds;
;     const int vb0 = (int)(unsigned)(uintptr_t)(lds + OFF_V) + v_rd_base(lane);
;     LAS float* wsl = (LAS float*)(lds + OFF_WS) + wid * 64; LAS float* li_l = wsl; LAS float* al_l = wsl + 32;
;     const float* cv_wgu = INF(layer == 0 ? 15 : 27); const float* cv_wdn = INF(layer == 0 ? 16 : 28); bf16* cv_gut = WSP(bf16, CV_MODE >= 2 ? WS_Q : WS_W_GUT); bf16* cv_dt = WSP(bf16, CV_MODE >= 2 ? WS_Q : WS_W_DT);
;     constexpr int CV_IG = 32 * 32, CV_ID = 8 * 64, CV_NIT = NEXP * (CV_IG + CV_ID);
;     int cv_it = (CV_MODE == 1) ? CV_NIT : bx * 4 + wid, cv_pend = -1; const int cv_stride = G * 4;
;     const unsigned cv_lds = (unsigned)(uintptr_t)(lds + OFF_CV) + (unsigned)(wid & 3) * 16384u;
.LBB0_1417:
	s_or_b64 exec, exec, s[4:5]
	s_mov_b32 s0, 30
	s_waitcnt lgkmcnt(0)
	s_barrier
	s_ashr_i32 s1, s0, 31
	s_lshl_b64 s[0:1], s[0:1], 3
	s_add_u32 s0, s80, s0
	s_addc_u32 s1, s81, s1
	s_load_dwordx2 s[4:5], s[0:1], 0x0
	v_mov_b32_e32 v4, v0
	s_mov_b32 s2, s78
	s_mov_b32 s9, s79
	s_mov_b32 s6, 20
	s_mov_b32 s0, 1
	s_mov_b32 s17, 0
	v_readfirstlane_b32 s0, v4
	s_ashr_i32 s3, s0, 6
	s_mov_b32 s0, 27
	s_ashr_i32 s1, s0, 31
	s_lshl_b64 s[0:1], s[0:1], 3
	s_add_u32 s0, s80, s0
	s_addc_u32 s1, s81, s1
	s_load_dwordx2 s[12:13], s[0:1], 0x0
	s_mov_b32 s0, 28
	s_ashr_i32 s1, s0, 31
	s_lshl_b64 s[0:1], s[0:1], 3
	s_add_u32 s0, s80, s0
	s_addc_u32 s1, s81, s1
	s_waitcnt lgkmcnt(0)
	s_add_u32 s60, s4, 0x3e00000
	s_addc_u32 s61, s5, 0
	s_add_u32 s62, s4, 0x13e00000
	s_load_dwordx2 s[14:15], s[0:1], 0x0
	s_addc_u32 s63, s5, 0
	s_lshl_b32 s0, s9, 2
	s_and_b32 s98, s3, 3
	s_add_i32 s73, s98, s0
	s_lshl_b32 s0, s3, 14
	s_and_b32 s0, s0, 0xc000
	s_add_i32 s10, s0, 0
	s_lshl_b32 s64, s2, 2
	s_add_i32 s65, s10, 0x15000
	s_cmpk_gt_i32 s9, 0x1ff
	s_mov_b32 s70, -1
	v_writelane_b32 v252, s2, 9
	s_cbranch_scc1 .LBB0_1477
	s_add_u32 s18, s4, 0x1fe00000
	s_addc_u32 s19, s5, 0
	v_lshrrev_b32_e32 v1, 4, v4
	v_and_b32_e32 v2, 15, v4
	s_add_u32 s0, s4, 0x42000000
	v_bitop3_b32 v1, v1, v2, 15 bitop3:0x6c
	v_lshlrev_b32_e32 v2, 10, v4
	v_writelane_b32 v252, s0, 13
	s_addc_u32 s0, s5, 0
	s_ashr_i32 s7, s6, 31
	v_and_b32_e32 v2, 0x3c000, v2
	v_writelane_b32 v252, s0, 14
	s_lshl_b64 s[0:1], s[6:7], 3
	v_lshl_or_b32 v1, v1, 4, v2
	v_lshrrev_b32_e32 v2, 5, v4
	v_lshrrev_b32_e32 v5, 1, v4
	s_add_u32 s0, s80, s0
	v_and_b32_e32 v2, 4, v2
	v_bfe_u32 v3, v4, 2, 2
	v_and_b32_e32 v5, 8, v5
	s_addc_u32 s1, s81, s1
	v_or3_b32 v2, v3, v5, v2
	v_and_b32_e32 v3, 0x60, v4
	v_lshlrev_b32_e32 v5, 3, v4
	s_add_u32 s2, s4, 0x5e200000
	v_and_or_b32 v3, v5, 24, v3
	v_writelane_b32 v252, s2, 15
	s_addc_u32 s2, s5, 0
	v_bfe_u32 v7, v4, 5, 1
	v_lshlrev_b32_e32 v3, 1, v3
	s_lshl_b32 s6, s3, 5
	v_and_b32_e32 v132, 31, v4
	v_lshl_or_b32 v133, v2, 14, v3
	v_bitop3_b32 v2, v7, v4, 15 bitop3:0x78
	s_cmp_gt_i32 s3, 3
	v_writelane_b32 v252, s2, 16
	v_lshlrev_b32_e32 v2, 4, v2
	v_lshlrev_b32_e32 v3, 7, v132
	s_movk_i32 s2, 0x4000
	s_cselect_b64 s[20:21], -1, 0
	s_lshl_b32 s76, s3, 10
	v_and_b32_e32 v6, 63, v4
	s_load_dwordx2 s[0:1], s[0:1], 0x0
	v_or3_b32 v173, v2, v3, s2
	v_lshlrev_b32_e32 v3, 4, v4
	s_add_i32 s76, s76, 0
	v_lshl_or_b32 v172, v132, 8, v2
	v_xor_b32_e32 v206, 32, v172
	v_xor_b32_e32 v207, 64, v172
	v_xor_b32_e32 v237, 0x60, v172
	v_xor_b32_e32 v244, 0x80, v172
	v_xor_b32_e32 v245, 0xa0, v172
	v_xor_b32_e32 v246, 0xc0, v172
	v_xor_b32_e32 v247, 0xe0, v172
	v_lshlrev_b32_e32 v2, 3, v6
	v_and_b32_e32 v3, 0xc0, v3
	v_lshlrev_b32_e32 v5, 1, v4
	s_add_i32 s77, s76, 0x7000
	s_add_i32 s78, s76, 0xfffff000
	v_and_or_b32 v3, v2, 24, v3
	v_and_b32_e32 v5, 32, v5
	v_and_b32_e32 v2, 0x100, v2
	s_cmp_eq_u32 s3, 4
	v_or3_b32 v2, v3, v5, v2
	v_mov_b32_e32 v3, 0
	v_writelane_b32 v252, s18, 26
	s_cselect_b64 s[4:5], -1, 0
	s_add_i32 s79, s76, 0xb000
	s_add_i32 s80, s76, 0x3000
	v_writelane_b32 v252, s19, 27
	v_and_b32_e32 v4, 32, v4
	v_mov_b32_e32 v5, v3
	s_cmp_lt_i32 s3, 4
	v_add_u32_e32 v174, 0, v2
	v_lshlrev_b32_e32 v2, 4, v7
	s_waitcnt lgkmcnt(0)
	v_lshl_add_u64 v[136:137], s[0:1], 0, v[4:5]
	v_writelane_b32 v252, s3, 18
	s_cselect_b64 s[24:25], -1, 0
	s_add_i32 s81, 0, 0x10800
	v_mul_i32_i24_e32 v4, -4, v7
	s_add_i32 s83, 0, 0x10900
	s_movk_i32 s74, 0x60
	v_lshl_add_u64 v[134:135], s[18:19], 0, v[2:3]
	v_lshlrev_b32_e32 v175, 2, v6
	v_add_u32_e32 v176, s81, v2
	s_add_i32 s82, s10, 0x17000
	v_add_u32_e32 v177, s83, v2
	v_or_b32_e32 v178, 0x40000, v1
	s_add_i32 s84, s76, 0x8000
	v_or_b32_e32 v179, 0x80000, v1
	s_add_i32 s85, s76, 0x9000
	v_or_b32_e32 v180, 0xc0000, v1
	s_add_i32 s86, s76, 0xa000
	v_or_b32_e32 v181, 0x40000, v133
	v_or_b32_e32 v182, 0x80000, v133
	s_add_i32 s87, s76, 0x1000
	v_or_b32_e32 v183, 0xc0000, v133
	s_add_i32 s88, s76, 0x2000
	s_add_i32 s89, s76, 0xc000
	s_add_i32 s90, s76, 0xd000
	s_add_i32 s91, s76, 0xe000
	s_add_i32 s92, s76, 0x4000
	s_add_i32 s93, s76, 0x5000
	s_add_i32 s94, s76, 0x6000
	s_add_i32 s95, s10, 0x15400
	s_add_i32 s96, s10, 0x15800
	s_add_i32 s97, s10, 0x15c00
	s_add_i32 s30, s10, 0x16000
	s_add_i32 s31, s10, 0x16400
	s_add_i32 s22, s10, 0x16800
	s_add_i32 s23, s10, 0x16c00
	s_add_i32 s28, s10, 0x17400
	s_add_i32 s29, s10, 0x17800
	s_add_i32 s33, s10, 0x17c00
	s_add_i32 s3, s10, 0x18000
	s_add_i32 s2, s10, 0x18400
	s_add_i32 s67, s10, 0x18800
	v_writelane_b32 v252, s10, 17
	s_add_i32 s66, s10, 0x18c00
	v_add3_u32 v184, v4, s6, v132
	v_mov_b32_e32 v185, 0x358637bd
	v_cndmask_b32_e64 v186, 0, 1, s[20:21]
	s_movk_i32 s1, 0x3ff
	s_movk_i32 s0, 0x70
	s_movk_i32 s26, 0x50
	s_mov_b32 s27, 0x42800000
	v_cndmask_b32_e64 v187, 0, 1, s[4:5]
	v_mov_b32_e32 v188, 0x10000
	v_mov_b32_e32 v189, 0xff800000
	v_writelane_b32 v252, s6, 23
	s_branch .LBB0_1420

.LBB0_1433:
	v_cndmask_b32_e64 v2, 0, 1, s[24:25]
	v_cmp_ne_u32_e64 s[8:9], 1, v2
	s_andn2_b64 vcc, exec, s[24:25]
	s_cmp_lt_i32 s70, 0
	s_cbranch_scc0 .LBB0_1446
	s_cmp_gt_i32 s73, 0x17fff
	s_cbranch_scc1 .LBB0_1447
.LBB0_1436:
	s_and_b64 vcc, exec, s[24:25]
	s_add_i32 s42, s73, 0xffff0000
	s_cmp_lt_i32 s73, 0x10000
	s_cselect_b32 s43, s73, s42
	s_cselect_b32 s44, s1, 0x1ff
	s_cselect_b32 s45, 10, 11
	s_cselect_b32 s42, 10, 9
	s_cselect_b32 s46, s13, s15
	s_cselect_b32 s47, s12, s14
	s_cselect_b32 s58, 21, 20
	s_and_b32 s44, s43, s44
	s_add_i32 s59, s45, -5
	s_ashr_i32 s42, s43, s42
	s_lshr_b32 s44, s44, s59
	s_lshl_b32 s59, -1, s59
	s_andn2_b32 s59, s43, s59
	s_ashr_i32 s43, s42, 31
	s_lshl_b64 s[42:43], s[42:43], s58
	s_lshl_b32 s44, s44, 6
	s_lshl_b64 s[42:43], s[42:43], 2
	s_add_u32 s42, s47, s42
	s_addc_u32 s43, s46, s43
	s_lshl_b32 s44, s44, s45
	v_mov_b32_e32 v2, v0
	s_lshl_b32 s44, s44, 2
	s_add_u32 s42, s42, s44
	v_bfe_u32 v68, v2, 3, 3
	v_lshlrev_b32_e32 v68, s45, v68
	s_addc_u32 s43, s43, 0
	s_lshl_b32 s44, s59, 7
	v_lshlrev_b32_e32 v2, 4, v2
	v_lshlrev_b32_e32 v68, 2, v68
	s_add_u32 s42, s42, s44
	v_and_b32_e32 v69, 0x70, v2
	s_addc_u32 s43, s43, 0
	v_or_b32_e32 v70, v68, v69
	s_cbranch_vccnz .Lcvs_a1b0_0
	s_mov_b32 s44, m0
	s_mov_b32 m0, s65
	s_nop 0
	global_load_lds_dwordx4 v70, s[42:43] nt
	s_mov_b32 m0, s44
.Lcvs_a1b0_0:
	s_lshl_b32 s44, 32, s45
	s_add_u32 s58, s42, s44
	s_addc_u32 s59, s43, 0
	v_bitop3_b32 v70, v68, 16, v69 bitop3:0x36
	s_cbranch_vccnz .Lcvs_a1b0_1
	s_mov_b32 s44, m0
	s_mov_b32 m0, s95
	s_nop 0
	global_load_lds_dwordx4 v70, s[58:59] nt
	s_mov_b32 m0, s44
.Lcvs_a1b0_1:
	s_lshl_b32 s44, 64, s45
	s_add_u32 s58, s42, s44
	s_addc_u32 s59, s43, 0
	v_bitop3_b32 v70, v68, 32, v69 bitop3:0x36
	s_cbranch_vccnz .Lcvs_a1b0_2
	s_mov_b32 s44, m0
	s_mov_b32 m0, s96
	s_nop 0
	global_load_lds_dwordx4 v70, s[58:59] nt
	s_mov_b32 m0, s44
.Lcvs_a1b0_2:
	s_lshl_b32 s44, 0x60, s45
	s_add_u32 s58, s42, s44
	s_addc_u32 s59, s43, 0
	v_bitop3_b32 v70, v68, 48, v69 bitop3:0x36
	s_cbranch_vccnz .Lcvs_a1b0_3
	s_mov_b32 s44, m0
	s_mov_b32 m0, s97
	s_nop 0
	global_load_lds_dwordx4 v70, s[58:59] nt
	s_mov_b32 m0, s44
.Lcvs_a1b0_3:
	s_lshl_b32 s44, 0x80, s45
	s_add_u32 s58, s42, s44
	s_addc_u32 s59, s43, 0
	v_bitop3_b32 v70, v68, 64, v69 bitop3:0x36
	s_cbranch_vccnz .Lcvs_a1b0_4
	s_mov_b32 s44, m0
	s_mov_b32 m0, s30
	s_nop 0
	global_load_lds_dwordx4 v70, s[58:59] nt
	s_mov_b32 m0, s44
.Lcvs_a1b0_4:
	s_lshl_b32 s44, 0xa0, s45
	s_add_u32 s58, s42, s44
	s_addc_u32 s59, s43, 0
	v_bitop3_b32 v70, v68, s26, v69 bitop3:0x36
	s_cbranch_vccnz .Lcvs_a1b0_5
	s_mov_b32 s44, m0
	s_mov_b32 m0, s31
	s_nop 0
	global_load_lds_dwordx4 v70, s[58:59] nt
	s_mov_b32 m0, s44
.Lcvs_a1b0_5:
	s_lshl_b32 s44, 0xc0, s45
	s_add_u32 s58, s42, s44
	s_addc_u32 s59, s43, 0
	v_bitop3_b32 v69, v68, s74, v69 bitop3:0x36
	s_cbranch_vccnz .Lcvs_a1b0_6
	s_mov_b32 s44, m0
	s_mov_b32 m0, s22
	s_nop 0
	global_load_lds_dwordx4 v69, s[58:59] nt
	s_mov_b32 m0, s44
.Lcvs_a1b0_6:
	s_lshl_b32 s44, 0xe0, s45
	s_add_u32 s42, s42, s44
	s_addc_u32 s43, s43, 0
	v_bitop3_b32 v2, v68, s0, v2 bitop3:0x34
	s_cbranch_vccnz .Lcvs_a1b0_7
	s_mov_b32 s44, m0
	s_mov_b32 m0, s23
	s_nop 0
	global_load_lds_dwordx4 v2, s[42:43] nt
	s_mov_b32 m0, s44
.Lcvs_a1b0_7:
	s_add_i32 s72, s73, s64
	s_mov_b32 s70, s73
	s_sub_i32 s42, s18, 63
	s_cmp_gt_i32 s42, s75
	s_cbranch_scc0 .LBB0_1448

.LBB0_1442:
	s_and_b64 vcc, exec, s[8:9]
	s_cmp_lt_i32 s70, 0
	s_cbranch_scc0 .LBB0_1461
	s_cmp_gt_i32 s72, 0x17fff
	s_cbranch_scc1 .LBB0_1462
.LBB0_1445:
	s_and_b64 vcc, exec, s[24:25]
	s_add_i32 s8, s72, 0xffff0000
	s_cmp_lt_i32 s72, 0x10000
	s_cselect_b32 s9, s72, s8
	s_cselect_b32 s42, s1, 0x1ff
	s_cselect_b32 s44, 10, 11
	s_cselect_b32 s8, 10, 9
	s_cselect_b32 s43, s13, s15
	s_cselect_b32 s45, s12, s14
	s_cselect_b32 s46, 21, 20
	s_and_b32 s42, s9, s42
	s_add_i32 s47, s44, -5
	s_ashr_i32 s8, s9, s8
	s_lshr_b32 s42, s42, s47
	s_lshl_b32 s47, -1, s47
	s_andn2_b32 s47, s9, s47
	s_ashr_i32 s9, s8, 31
	s_lshl_b64 s[8:9], s[8:9], s46
	s_lshl_b32 s42, s42, 6
	s_lshl_b64 s[8:9], s[8:9], 2
	s_add_u32 s8, s45, s8
	s_addc_u32 s9, s43, s9
	s_lshl_b32 s42, s42, s44
	v_mov_b32_e32 v2, v0
	s_lshl_b32 s42, s42, 2
	s_add_u32 s8, s8, s42
	v_bfe_u32 v68, v2, 3, 3
	v_lshlrev_b32_e32 v68, s44, v68
	s_addc_u32 s9, s9, 0
	s_lshl_b32 s42, s47, 7
	v_lshlrev_b32_e32 v2, 4, v2
	v_lshlrev_b32_e32 v68, 2, v68
	s_add_u32 s8, s8, s42
	v_and_b32_e32 v69, 0x70, v2
	s_addc_u32 s9, s9, 0
	v_or_b32_e32 v70, v68, v69
	s_cbranch_vccnz .Lcvs_a1b1_0
	s_mov_b32 s42, m0
	s_mov_b32 m0, s82
	s_nop 0
	global_load_lds_dwordx4 v70, s[8:9] nt
	s_mov_b32 m0, s42
.Lcvs_a1b1_0:
	s_lshl_b32 s42, 32, s44
	s_add_u32 s42, s8, s42
	s_addc_u32 s43, s9, 0
	v_bitop3_b32 v70, v68, 16, v69 bitop3:0x36
	s_cbranch_vccnz .Lcvs_a1b1_1
	s_mov_b32 s45, m0
	s_mov_b32 m0, s28
	s_nop 0
	global_load_lds_dwordx4 v70, s[42:43] nt
	s_mov_b32 m0, s45
.Lcvs_a1b1_1:
	s_lshl_b32 s42, 64, s44
	s_add_u32 s42, s8, s42
	s_addc_u32 s43, s9, 0
	v_bitop3_b32 v70, v68, 32, v69 bitop3:0x36
	s_cbranch_vccnz .Lcvs_a1b1_2
	s_mov_b32 s45, m0
	s_mov_b32 m0, s29
	s_nop 0
	global_load_lds_dwordx4 v70, s[42:43] nt
	s_mov_b32 m0, s45
.Lcvs_a1b1_2:
	s_lshl_b32 s42, 0x60, s44
	s_add_u32 s42, s8, s42
	s_addc_u32 s43, s9, 0
	v_bitop3_b32 v70, v68, 48, v69 bitop3:0x36
	s_cbranch_vccnz .Lcvs_a1b1_3
	s_mov_b32 s45, m0
	s_mov_b32 m0, s33
	s_nop 0
	global_load_lds_dwordx4 v70, s[42:43] nt
	s_mov_b32 m0, s45
.Lcvs_a1b1_3:
	s_lshl_b32 s42, 0x80, s44
	s_add_u32 s42, s8, s42
	s_addc_u32 s43, s9, 0
	v_bitop3_b32 v70, v68, 64, v69 bitop3:0x36
	s_cbranch_vccnz .Lcvs_a1b1_4
	s_mov_b32 s45, m0
	s_mov_b32 m0, s3
	s_nop 0
	global_load_lds_dwordx4 v70, s[42:43] nt
	s_mov_b32 m0, s45
.Lcvs_a1b1_4:
	s_lshl_b32 s42, 0xa0, s44
	s_add_u32 s42, s8, s42
	s_addc_u32 s43, s9, 0
	v_bitop3_b32 v70, v68, s26, v69 bitop3:0x36
	s_cbranch_vccnz .Lcvs_a1b1_5
	s_mov_b32 s45, m0
	s_mov_b32 m0, s2
	s_nop 0
	global_load_lds_dwordx4 v70, s[42:43] nt
	s_mov_b32 m0, s45
.Lcvs_a1b1_5:
	s_lshl_b32 s42, 0xc0, s44
	s_add_u32 s42, s8, s42
	s_addc_u32 s43, s9, 0
	v_bitop3_b32 v69, v68, s74, v69 bitop3:0x36
	s_cbranch_vccnz .Lcvs_a1b1_6
	s_mov_b32 s45, m0
	s_mov_b32 m0, s67
	s_nop 0
	global_load_lds_dwordx4 v69, s[42:43] nt
	s_mov_b32 m0, s45
.Lcvs_a1b1_6:
	s_lshl_b32 s42, 0xe0, s44
	s_add_u32 s8, s8, s42
	s_addc_u32 s9, s9, 0
	v_bitop3_b32 v2, v68, s0, v2 bitop3:0x34
	s_cbranch_vccnz .Lcvs_a1b1_7
	s_mov_b32 s42, m0
	s_mov_b32 m0, s66
	s_nop 0
	global_load_lds_dwordx4 v2, s[8:9] nt
	s_mov_b32 m0, s42
.Lcvs_a1b1_7:
	s_add_i32 s73, s72, s64
	s_mov_b32 s70, s72
	s_add_i32 s8, s18, 1
	s_cmp_gt_i32 s8, s75
	s_cbranch_scc1 .LBB0_1426
	s_branch .LBB0_1463
.Lfsk_a1b0:
	s_mov_b32 s70, -1
	s_cmp_gt_i32 s73, 0x17fff
	s_cbranch_scc0 .LBB0_1436
	s_branch .LBB0_1447
.LBB0_1446:
	s_and_b64 vcc, exec, s[20:21]
	s_cbranch_vccnz .Lfsk_a1b0
	v_sub_co_u32_e32 v2, vcc, s70, v188
	s_and_b64 s[58:59], vcc, exec
	v_readfirstlane_b32 s42, v2
	s_cselect_b32 s42, s70, s42
	s_cselect_b32 s58, s1, 0x1ff
	s_cselect_b32 s43, 10, 9
	s_and_b32 s72, s42, s58
	v_mov_b32_e32 v142, v0
	s_waitcnt vmcnt(0)
	s_and_b64 s[58:59], vcc, exec
	s_cselect_b32 s58, 5, 6
	v_and_b32_e32 v2, 7, v142
	v_lshrrev_b32_e32 v68, 3, v142
	v_bfe_u32 v140, v142, 3, 2
	v_lshlrev_b32_e32 v69, 10, v2
	v_lshlrev_b32_e32 v70, 2, v2
	v_and_b32_e32 v71, 4, v68
	v_lshlrev_b32_e32 v72, 2, v140
	s_lshr_b32 s72, s72, s58
	s_lshl_b32 s58, -1, s58
	v_add3_u32 v69, s65, v69, v72
	v_bitop3_b32 v72, v71, v70, 8 bitop3:0x36
	s_andn2_b32 s44, s42, s58
	v_bitop3_b32 v68, v68, v70, 4 bitop3:0x6c
	v_lshl_add_u32 v76, v72, 2, v69
	v_bitop3_b32 v72, v71, v70, 16 bitop3:0x36
	v_bitop3_b32 v70, v71, v70, 24 bitop3:0x36
	s_lshl_b32 s45, s44, 5
	v_lshl_add_u32 v68, v68, 2, v69
	v_lshl_add_u32 v84, v72, 2, v69
	v_lshl_add_u32 v92, v70, 2, v69
	s_and_b64 s[58:59], vcc, exec
	v_add_u32_e32 v74, 0x2000, v68
	v_add_u32_e32 v82, 0x2000, v76
	v_add_u32_e32 v90, 0x2000, v84
	v_add_u32_e32 v98, 0x2000, v92
	s_cselect_b32 s46, s61, s63
	s_cselect_b32 s47, s60, s62
	s_ashr_i32 s58, s42, s43
	ds_read2_b32 v[68:69], v74 offset1:32
	ds_read2_b32 v[70:71], v74 offset0:64 offset1:96
	ds_read2_b32 v[72:73], v74 offset0:128 offset1:160
	ds_read2_b32 v[74:75], v74 offset0:192 offset1:224
	ds_read2_b32 v[76:77], v82 offset1:32
	ds_read2_b32 v[78:79], v82 offset0:64 offset1:96
	ds_read2_b32 v[80:81], v82 offset0:128 offset1:160
	ds_read2_b32 v[82:83], v82 offset0:192 offset1:224
	ds_read2_b32 v[84:85], v90 offset1:32
	ds_read2_b32 v[86:87], v90 offset0:64 offset1:96
	ds_read2_b32 v[88:89], v90 offset0:128 offset1:160
	ds_read2_b32 v[90:91], v90 offset0:192 offset1:224
	ds_read2_b32 v[92:93], v98 offset1:32
	ds_read2_b32 v[94:95], v98 offset0:64 offset1:96
	ds_read2_b32 v[96:97], v98 offset0:128 offset1:160
	ds_read2_b32 v[98:99], v98 offset0:192 offset1:224
	s_ashr_i32 s59, s58, 31
	s_and_b64 s[42:43], vcc, exec
	s_cselect_b32 s42, 21, 20
	s_lshl_b64 s[42:43], s[58:59], s42
	s_waitcnt lgkmcnt(0)
	s_lshl_b64 s[42:43], s[42:43], 1
	s_add_u32 s42, s47, s42
	v_bfe_u32 v143, v142, 3, 3
	s_addc_u32 s43, s46, s43
	s_lshl_b32 s46, s44, 6
	s_lshl_b32 s58, s70, 6
	s_and_b32 s47, s46, 0x300
	s_and_b32 s58, s58, 0x80
	s_lshr_b32 s44, s44, 2
	s_or_b32 s47, s47, s58
	s_and_b32 s44, s44, 28
	s_or_b32 s44, s47, s44
	v_or_b32_e32 v144, s44, v140
	s_lshl_b32 s44, s72, 7
	s_add_u32 s42, s42, s44
	s_addc_u32 s43, s43, 0
	v_lshlrev_b32_e32 v2, 4, v2
	v_lshl_add_u64 v[140:141], s[42:43], 0, v[2:3]
	v_lshrrev_b32_e32 v2, 2, v142
	v_and_b32_e32 v2, 8, v2
	s_waitcnt lgkmcnt(14)
	v_cvt_pk_bf16_f32 v68, v68, v69
	v_cvt_pk_bf16_f32 v69, v70, v71
	s_waitcnt lgkmcnt(12)
	v_cvt_pk_bf16_f32 v71, v74, v75
	s_and_b32 s44, s46, 64
	v_add_u32_e32 v75, v144, v2
	v_or_b32_e32 v74, s45, v143
	v_or_b32_e32 v2, s44, v75
	s_and_b64 s[42:43], vcc, exec
	v_cndmask_b32_e32 v2, v74, v2, vcc
	s_cselect_b32 s42, 11, 9
	v_cvt_pk_bf16_f32 v70, v72, v73
	v_lshlrev_b64 v[72:73], s42, v[2:3]
	v_lshl_add_u64 v[72:73], v[72:73], 1, v[140:141]
	v_or_b32_e32 v2, 8, v143
	global_store_dwordx4 v[72:73], v[68:71], off nt
	v_or_b32_e32 v72, s45, v2
	v_lshlrev_b32_e32 v2, 1, v2
	v_and_b32_e32 v2, 24, v2
	v_add_u32_e32 v2, v2, v144
	v_or_b32_e32 v2, s44, v2
	v_cndmask_b32_e32 v2, v72, v2, vcc
	v_lshlrev_b64 v[72:73], s42, v[2:3]
	v_lshl_add_u64 v[72:73], v[72:73], 1, v[140:141]
	v_or_b32_e32 v2, 16, v74
	s_waitcnt lgkmcnt(11)
	v_cvt_pk_bf16_f32 v68, v76, v77
	s_waitcnt lgkmcnt(10)
	v_cvt_pk_bf16_f32 v69, v78, v79
	s_waitcnt lgkmcnt(9)
	v_cvt_pk_bf16_f32 v70, v80, v81
	s_waitcnt lgkmcnt(8)
	v_cvt_pk_bf16_f32 v71, v82, v83
	global_store_dwordx4 v[72:73], v[68:71], off nt
	v_lshlrev_b32_e32 v72, 1, v2
	v_and_b32_e32 v72, 0x60, v72
	v_add_u32_e32 v72, v75, v72
	v_cndmask_b32_e32 v2, v2, v72, vcc
	v_lshlrev_b64 v[72:73], s42, v[2:3]
	v_lshl_add_u64 v[72:73], v[72:73], 1, v[140:141]
	v_or_b32_e32 v2, 24, v143
	s_waitcnt lgkmcnt(7)
	v_cvt_pk_bf16_f32 v68, v84, v85
	s_waitcnt lgkmcnt(6)
	v_cvt_pk_bf16_f32 v69, v86, v87
	s_waitcnt lgkmcnt(5)
	v_cvt_pk_bf16_f32 v70, v88, v89
	s_waitcnt lgkmcnt(4)
	v_cvt_pk_bf16_f32 v71, v90, v91
	global_store_dwordx4 v[72:73], v[68:71], off nt
	v_or_b32_e32 v72, s45, v2
	v_lshlrev_b32_e32 v73, 1, v72
	v_lshlrev_b32_e32 v2, 1, v2
	v_and_b32_e32 v73, 0x60, v73
	v_and_b32_e32 v2, 24, v2
	v_add3_u32 v2, v2, v144, v73
	v_cndmask_b32_e32 v2, v72, v2, vcc
	v_lshlrev_b64 v[72:73], s42, v[2:3]
	v_lshl_add_u64 v[72:73], v[72:73], 1, v[140:141]
	s_mov_b32 s70, -1
	s_waitcnt lgkmcnt(3)
	v_cvt_pk_bf16_f32 v68, v92, v93
	s_waitcnt lgkmcnt(2)
	v_cvt_pk_bf16_f32 v69, v94, v95
	s_waitcnt lgkmcnt(1)
	v_cvt_pk_bf16_f32 v70, v96, v97
	s_waitcnt lgkmcnt(0)
	v_cvt_pk_bf16_f32 v71, v98, v99
	global_store_dwordx4 v[72:73], v[68:71], off nt
	s_cmp_gt_i32 s73, 0x17fff
	s_cbranch_scc0 .LBB0_1436

.Lfsk_a1b1:
	s_mov_b32 s70, -1
	s_cmp_gt_i32 s72, 0x17fff
	s_cbranch_scc0 .LBB0_1445
	s_branch .LBB0_1462
.LBB0_1461:
	s_and_b64 vcc, exec, s[20:21]
	s_cbranch_vccnz .Lfsk_a1b1
	v_sub_co_u32_e32 v2, vcc, s70, v188
	s_and_b64 s[8:9], vcc, exec
	v_mov_b32_e32 v142, v0
	s_waitcnt vmcnt(0)
	v_readfirstlane_b32 s8, v2
	s_cselect_b32 s42, s70, s8
	v_and_b32_e32 v2, 7, v142
	v_bfe_u32 v140, v142, 3, 2
	v_lshrrev_b32_e32 v68, 3, v142
	v_lshlrev_b32_e32 v69, 10, v2
	v_lshlrev_b32_e32 v70, 2, v2
	v_lshlrev_b32_e32 v72, 2, v140
	v_and_b32_e32 v71, 4, v68
	v_add3_u32 v69, s65, v69, v72
	v_bitop3_b32 v68, v68, v70, 4 bitop3:0x6c
	v_lshl_add_u32 v74, v68, 2, v69
	v_bitop3_b32 v68, v71, v70, 8 bitop3:0x36
	v_lshl_add_u32 v82, v68, 2, v69
	v_bitop3_b32 v68, v71, v70, 16 bitop3:0x36
	v_lshl_add_u32 v90, v68, 2, v69
	v_bitop3_b32 v68, v71, v70, 24 bitop3:0x36
	v_lshl_add_u32 v98, v68, 2, v69
	ds_read2_b32 v[68:69], v74 offset1:32
	ds_read2_b32 v[70:71], v74 offset0:64 offset1:96
	ds_read2_b32 v[72:73], v74 offset0:128 offset1:160
	ds_read2_b32 v[74:75], v74 offset0:192 offset1:224
	ds_read2_b32 v[76:77], v82 offset1:32
	ds_read2_b32 v[78:79], v82 offset0:64 offset1:96
	ds_read2_b32 v[80:81], v82 offset0:128 offset1:160
	ds_read2_b32 v[82:83], v82 offset0:192 offset1:224
	ds_read2_b32 v[84:85], v90 offset1:32
	ds_read2_b32 v[86:87], v90 offset0:64 offset1:96
	ds_read2_b32 v[88:89], v90 offset0:128 offset1:160
	ds_read2_b32 v[90:91], v90 offset0:192 offset1:224
	ds_read2_b32 v[92:93], v98 offset1:32
	ds_read2_b32 v[94:95], v98 offset0:64 offset1:96
	ds_read2_b32 v[96:97], v98 offset0:128 offset1:160
	ds_read2_b32 v[98:99], v98 offset0:192 offset1:224
	s_cselect_b32 s8, s1, 0x1ff
	s_cselect_b32 s43, 10, 9
	s_and_b32 s44, s42, s8
	s_and_b64 s[8:9], vcc, exec
	s_cselect_b32 s8, 5, 6
	s_lshr_b32 s44, s44, s8
	s_lshl_b32 s8, -1, s8
	s_andn2_b32 s45, s42, s8
	s_lshl_b32 s46, s45, 5
	s_and_b64 s[8:9], vcc, exec
	s_cselect_b32 s47, s61, s63
	s_cselect_b32 s58, s60, s62
	s_ashr_i32 s8, s42, s43
	s_ashr_i32 s9, s8, 31
	s_and_b64 s[42:43], vcc, exec
	s_cselect_b32 s42, 21, 20
	s_lshl_b64 s[8:9], s[8:9], s42
	s_waitcnt lgkmcnt(0)
	s_lshl_b64 s[8:9], s[8:9], 1
	s_add_u32 s8, s58, s8
	v_bfe_u32 v143, v142, 3, 3
	s_addc_u32 s9, s47, s9
	s_lshl_b32 s42, s45, 6
	s_lshl_b32 s47, s70, 6
	s_and_b32 s43, s42, 0x300
	s_and_b32 s47, s47, 0x80
	s_lshr_b32 s45, s45, 2
	s_or_b32 s43, s43, s47
	s_and_b32 s45, s45, 28
	s_or_b32 s43, s43, s45
	v_or_b32_e32 v144, s43, v140
	s_lshl_b32 s43, s44, 7
	s_add_u32 s8, s8, s43
	s_addc_u32 s9, s9, 0
	v_lshlrev_b32_e32 v2, 4, v2
	v_lshl_add_u64 v[140:141], s[8:9], 0, v[2:3]
	v_lshrrev_b32_e32 v2, 2, v142
	v_and_b32_e32 v2, 8, v2
	s_waitcnt lgkmcnt(14)
	v_cvt_pk_bf16_f32 v68, v68, v69
	v_cvt_pk_bf16_f32 v69, v70, v71
	s_waitcnt lgkmcnt(12)
	v_cvt_pk_bf16_f32 v71, v74, v75
	s_and_b32 s42, s42, 64
	v_add_u32_e32 v75, v144, v2
	v_or_b32_e32 v74, s46, v143
	v_or_b32_e32 v2, s42, v75
	s_and_b64 s[8:9], vcc, exec
	v_cndmask_b32_e32 v2, v74, v2, vcc
	s_cselect_b32 s8, 11, 9
	v_cvt_pk_bf16_f32 v70, v72, v73
	v_lshlrev_b64 v[72:73], s8, v[2:3]
	v_lshl_add_u64 v[72:73], v[72:73], 1, v[140:141]
	v_or_b32_e32 v2, 8, v143
	global_store_dwordx4 v[72:73], v[68:71], off nt
	v_or_b32_e32 v72, s46, v2
	v_lshlrev_b32_e32 v2, 1, v2
	v_and_b32_e32 v2, 24, v2
	v_add_u32_e32 v2, v2, v144
	v_or_b32_e32 v2, s42, v2
	v_cndmask_b32_e32 v2, v72, v2, vcc
	v_lshlrev_b64 v[72:73], s8, v[2:3]
	v_lshl_add_u64 v[72:73], v[72:73], 1, v[140:141]
	v_or_b32_e32 v2, 16, v74
	s_waitcnt lgkmcnt(11)
	v_cvt_pk_bf16_f32 v68, v76, v77
	s_waitcnt lgkmcnt(10)
	v_cvt_pk_bf16_f32 v69, v78, v79
	s_waitcnt lgkmcnt(9)
	v_cvt_pk_bf16_f32 v70, v80, v81
	s_waitcnt lgkmcnt(8)
	v_cvt_pk_bf16_f32 v71, v82, v83
	global_store_dwordx4 v[72:73], v[68:71], off nt
	v_lshlrev_b32_e32 v72, 1, v2
	v_and_b32_e32 v72, 0x60, v72
	v_add_u32_e32 v72, v75, v72
	v_cndmask_b32_e32 v2, v2, v72, vcc
	v_lshlrev_b64 v[72:73], s8, v[2:3]
	v_lshl_add_u64 v[72:73], v[72:73], 1, v[140:141]
	v_or_b32_e32 v2, 24, v143
	s_waitcnt lgkmcnt(7)
	v_cvt_pk_bf16_f32 v68, v84, v85
	s_waitcnt lgkmcnt(6)
	v_cvt_pk_bf16_f32 v69, v86, v87
	s_waitcnt lgkmcnt(5)
	v_cvt_pk_bf16_f32 v70, v88, v89
	s_waitcnt lgkmcnt(4)
	v_cvt_pk_bf16_f32 v71, v90, v91
	global_store_dwordx4 v[72:73], v[68:71], off nt
	v_or_b32_e32 v72, s46, v2
	v_lshlrev_b32_e32 v73, 1, v72
	v_lshlrev_b32_e32 v2, 1, v2
	v_and_b32_e32 v73, 0x60, v73
	v_and_b32_e32 v2, 24, v2
	v_add3_u32 v2, v2, v144, v73
	v_cndmask_b32_e32 v2, v72, v2, vcc
	v_lshlrev_b64 v[72:73], s8, v[2:3]
	v_lshl_add_u64 v[72:73], v[72:73], 1, v[140:141]
	s_mov_b32 s70, -1
	s_waitcnt lgkmcnt(3)
	v_cvt_pk_bf16_f32 v68, v92, v93
	s_waitcnt lgkmcnt(2)
	v_cvt_pk_bf16_f32 v69, v94, v95
	s_waitcnt lgkmcnt(1)
	v_cvt_pk_bf16_f32 v70, v96, v97
	s_waitcnt lgkmcnt(0)
	v_cvt_pk_bf16_f32 v71, v98, v99
	global_store_dwordx4 v[72:73], v[68:71], off nt
	s_cmp_gt_i32 s72, 0x17fff
	s_cbranch_scc0 .LBB0_1445
